# layer-0 out-proj epilogue: residual f32 loads and bf16 row stores lane-transposed through ds_bpermute (quad of lanes = one row line)
# speedup vs baseline: 1.0153x; 1.0015x over previous
; #define PG8_RSRC(base) __builtin_amdgcn_make_buffer_rsrc((void*)(base), (short)0, -1, 0x00020000)
; #define PG8_ST16(rs, b0, p, v) __builtin_amdgcn_raw_buffer_store_b128(v, rs, (int)((const char*)(p) - (const char*)(b0)), 0, 16)
;     __device__ __forceinline__ void operator()(const f32x4 (&acc)[2][2][4][2], const Unit& u, int wr, int wc, int fr, int fq) const {
;         const int row0 = u.pm * BM + wr * 64 + fr, col0 = u.pn * BM + wc * 32 + 8 * fq; const __amdgpu_buffer_rsrc_t rs_ = PG8_RSRC(out);
; #pragma unroll
;         for (int ai = 0; ai < 2; ++ai) {
;             f32x4 b0[4][2], b1[4][2];
; #pragma unroll
;             for (int m = 0; m < 4; ++m) { const size_t off = (size_t)(row0 + ai * HALF + m * 16) * ldc + col0;
; #pragma unroll
;                 for (int bj = 0; bj < 2; ++bj) {
;                     if (BASE_F32) { b0[m][bj] = *(const f32x4*)((const float*)base + off + bj * HALF); b1[m][bj] = *(const f32x4*)((const float*)base + off + bj * HALF + 4); }
;                     else { const u32x4 q = *(const u32x4*)((const bf16_t*)base + off + bj * HALF);
;                         b0[m][bj] = (f32x4){__uint_as_float(q.x << 16), __uint_as_float(q.x & 0xffff0000u), __uint_as_float(q.y << 16), __uint_as_float(q.y & 0xffff0000u)};
;                         b1[m][bj] = (f32x4){__uint_as_float(q.z << 16), __uint_as_float(q.z & 0xffff0000u), __uint_as_float(q.w << 16), __uint_as_float(q.w & 0xffff0000u)}; } } }
;             asm volatile("" ::: "memory");
; #pragma unroll
;             for (int m = 0; m < 4; ++m) { const size_t off = (size_t)(row0 + ai * HALF + m * 16) * ldc + col0; float ssq = 0.f;
; #pragma unroll
;                 for (int bj = 0; bj < 2; ++bj) {
;                     const f32x4 o0 = b0[m][bj] + acc[ai][bj][m][0] * sc, o1 = b1[m][bj] + acc[ai][bj][m][1] * sc;
;                     ssq += ((o0[0] * o0[0] + o0[1] * o0[1]) + (o0[2] * o0[2] + o0[3] * o0[3])) + ((o1[0] * o1[0] + o1[1] * o1[1]) + (o1[2] * o1[2] + o1[3] * o1[3]));
;                     u32x4 w; w.x = cvt_pk_bf16(o0[0], o0[1]); w.y = cvt_pk_bf16(o0[2], o0[3]); w.z = cvt_pk_bf16(o1[0], o1[1]); w.w = cvt_pk_bf16(o1[2], o1[3]);
;                     PG8_ST16(rs_, out, out + off + bj * HALF, w); }
;                 ssq += __shfl_xor(ssq, 16); ssq += __shfl_xor(ssq, 32);
;                 if (fq == 0) rowss[(size_t)(row0 + ai * HALF + m * 16) * 32 + 4 * u.pn + wc] = ssq; }
.LBB0_871:
	v_lshrrev_b32_e32 v252, 2, v215
	v_and_b32_e32 v207, 15, v215
	v_sub_u32_e32 v252, v252, v207
	v_lshlrev_b32_e32 v207, 4, v207
	v_lshrrev_b32_e32 v249, 4, v215
	v_lshl_or_b32 v249, v249, 2, v207
	v_and_b32_e32 v207, 3, v215
	v_lshrrev_b32_e32 v248, 4, v215
	v_sub_u32_e32 v248, v207, v248
	v_lshlrev_b32_e32 v238, 12, v252
	v_lshl_add_u32 v238, v248, 4, v238
	v_ashrrev_i32_e32 v239, 31, v238
	v_lshlrev_b32_e32 v240, 1, v238
	v_ashrrev_i32_e32 v241, 31, v240
	v_and_b32_e32 v248, 60, v215
	v_lshl_or_b32 v248, v207, 6, v248
	v_lshl_add_u32 v194, s69, 8, v208
	v_lshl_or_b32 v190, s68, 8, v218
	v_ashrrev_i32_e32 v191, 31, v190
	v_ashrrev_i32_e32 v195, 31, v194
	v_lshl_add_u64 v[192:193], v[190:191], 2, s[18:19]
	v_lshl_add_u64 v[192:193], v[192:193], 0, v[240:241]
	v_lshlrev_b64 v[132:133], 13, v[194:195]
	v_lshl_add_u64 v[132:133], v[192:193], 0, v[132:133]
	global_load_dwordx4 v[198:201], v[132:133], off offset:16
	global_load_dwordx4 v[220:223], v[132:133], off
	global_load_dwordx4 v[224:227], v[132:133], off offset:528
	global_load_dwordx4 v[228:231], v[132:133], off offset:512
	v_or_b32_e32 v204, 16, v194
	v_ashrrev_i32_e32 v205, 31, v204
	v_lshlrev_b64 v[132:133], 13, v[204:205]
	v_or_b32_e32 v202, 32, v194
	v_lshl_add_u64 v[132:133], v[192:193], 0, v[132:133]
	v_ashrrev_i32_e32 v203, 31, v202
	global_load_dwordx4 v[172:175], v[132:133], off offset:16
	global_load_dwordx4 v[176:179], v[132:133], off
	global_load_dwordx4 v[164:167], v[132:133], off offset:528
	global_load_dwordx4 v[168:171], v[132:133], off offset:512
	v_lshlrev_b64 v[132:133], 13, v[202:203]
	v_or_b32_e32 v196, 48, v194
	v_lshl_add_u64 v[132:133], v[192:193], 0, v[132:133]
	v_ashrrev_i32_e32 v197, 31, v196
	global_load_dwordx4 v[156:159], v[132:133], off offset:16
	global_load_dwordx4 v[160:163], v[132:133], off
	global_load_dwordx4 v[140:143], v[132:133], off offset:528
	global_load_dwordx4 v[148:151], v[132:133], off offset:512
	v_lshlrev_b64 v[132:133], 13, v[196:197]
	v_lshl_add_u64 v[136:137], v[192:193], 0, v[132:133]
	global_load_dwordx4 v[144:147], v[136:137], off offset:16
	global_load_dwordx4 v[152:155], v[136:137], off
	global_load_dwordx4 v[132:135], v[136:137], off offset:528
	s_nop 0
	global_load_dwordx4 v[136:139], v[136:137], off offset:512
	s_lshl_b32 s42, s68, 2
	s_ashr_i32 s43, s42, 31
	s_waitcnt vmcnt(0)
	ds_bpermute_b32 v198, v249, v198
	ds_bpermute_b32 v199, v249, v199
	ds_bpermute_b32 v200, v249, v200
	ds_bpermute_b32 v201, v249, v201
	ds_bpermute_b32 v220, v249, v220
	ds_bpermute_b32 v221, v249, v221
	ds_bpermute_b32 v222, v249, v222
	ds_bpermute_b32 v223, v249, v223
	ds_bpermute_b32 v224, v249, v224
	ds_bpermute_b32 v225, v249, v225
	ds_bpermute_b32 v226, v249, v226
	ds_bpermute_b32 v227, v249, v227
	ds_bpermute_b32 v228, v249, v228
	ds_bpermute_b32 v229, v249, v229
	ds_bpermute_b32 v230, v249, v230
	ds_bpermute_b32 v231, v249, v231
	ds_bpermute_b32 v172, v249, v172
	ds_bpermute_b32 v173, v249, v173
	ds_bpermute_b32 v174, v249, v174
	ds_bpermute_b32 v175, v249, v175
	ds_bpermute_b32 v176, v249, v176
	ds_bpermute_b32 v177, v249, v177
	ds_bpermute_b32 v178, v249, v178
	ds_bpermute_b32 v179, v249, v179
	ds_bpermute_b32 v164, v249, v164
	ds_bpermute_b32 v165, v249, v165
	ds_bpermute_b32 v166, v249, v166
	ds_bpermute_b32 v167, v249, v167
	ds_bpermute_b32 v168, v249, v168
	ds_bpermute_b32 v169, v249, v169
	ds_bpermute_b32 v170, v249, v170
	ds_bpermute_b32 v171, v249, v171
	ds_bpermute_b32 v156, v249, v156
	ds_bpermute_b32 v157, v249, v157
	ds_bpermute_b32 v158, v249, v158
	ds_bpermute_b32 v159, v249, v159
	ds_bpermute_b32 v160, v249, v160
	ds_bpermute_b32 v161, v249, v161
	ds_bpermute_b32 v162, v249, v162
	ds_bpermute_b32 v163, v249, v163
	ds_bpermute_b32 v140, v249, v140
	ds_bpermute_b32 v141, v249, v141
	ds_bpermute_b32 v142, v249, v142
	ds_bpermute_b32 v143, v249, v143
	ds_bpermute_b32 v148, v249, v148
	ds_bpermute_b32 v149, v249, v149
	ds_bpermute_b32 v150, v249, v150
	ds_bpermute_b32 v151, v249, v151
	ds_bpermute_b32 v144, v249, v144
	ds_bpermute_b32 v145, v249, v145
	ds_bpermute_b32 v146, v249, v146
	ds_bpermute_b32 v147, v249, v147
	ds_bpermute_b32 v152, v249, v152
	ds_bpermute_b32 v153, v249, v153
	ds_bpermute_b32 v154, v249, v154
	ds_bpermute_b32 v155, v249, v155
	ds_bpermute_b32 v132, v249, v132
	ds_bpermute_b32 v133, v249, v133
	ds_bpermute_b32 v134, v249, v134
	ds_bpermute_b32 v135, v249, v135
	ds_bpermute_b32 v136, v249, v136
	ds_bpermute_b32 v137, v249, v137
	ds_bpermute_b32 v138, v249, v138
	ds_bpermute_b32 v139, v249, v139
	s_waitcnt lgkmcnt(0)
	v_pk_add_f32 v[128:129], v[128:129], v[198:199]
	v_pk_add_f32 v[126:127], v[126:127], v[222:223]
	v_pk_add_f32 v[124:125], v[124:125], v[220:221]
	v_mul_f32_e32 v199, v127, v127
	v_mul_f32_e32 v198, v125, v125
	v_fmac_f32_e32 v198, v124, v124
	v_fmac_f32_e32 v199, v126, v126
	v_add_f32_e32 v198, v198, v199
	v_mul_f32_e32 v199, v129, v129
	v_fmac_f32_e32 v199, v128, v128
	v_cvt_pk_bf16_f32 v124, v124, v125
	v_cvt_pk_bf16_f32 v125, v126, v127
	v_cvt_pk_bf16_f32 v126, v128, v129
	v_lshlrev_b64 v[128:129], 12, v[194:195]
	v_lshl_add_u64 v[128:129], s[20:21], 0, v[128:129]
	v_lshl_add_u64 v[128:129], v[190:191], 1, v[128:129]
	v_pk_add_f32 v[122:123], v[122:123], v[230:231]
	v_pk_add_f32 v[120:121], v[120:121], v[228:229]
	v_pk_add_f32 v[130:131], v[130:131], v[200:201]
	s_nop 0
	v_cvt_pk_bf16_f32 v127, v130, v131
	v_lshl_add_u64 v[234:235], v[128:129], 0, v[238:239]
	ds_bpermute_b32 v240, v248, v124
	ds_bpermute_b32 v241, v248, v125
	ds_bpermute_b32 v242, v248, v126
	ds_bpermute_b32 v243, v248, v127
	v_mul_f32_e32 v200, v131, v131
	v_fmac_f32_e32 v200, v130, v130
	v_pk_add_f32 v[124:125], v[118:119], v[226:227]
	v_pk_add_f32 v[118:119], v[116:117], v[224:225]
	v_mul_f32_e32 v116, v121, v121
	v_mul_f32_e32 v117, v123, v123
	v_fmac_f32_e32 v116, v120, v120
	v_fmac_f32_e32 v117, v122, v122
	v_add_f32_e32 v116, v116, v117
	v_mul_f32_e32 v117, v119, v119
	v_mul_f32_e32 v126, v125, v125
	v_fmac_f32_e32 v117, v118, v118
	v_fmac_f32_e32 v126, v124, v124
	v_add_f32_e32 v199, v199, v200
	v_add_f32_e32 v117, v117, v126
	v_add_f32_e32 v198, v198, v199
	v_add_f32_e32 v116, v116, v117
	v_add_f32_e32 v126, v198, v116
	v_cvt_pk_bf16_f32 v116, v120, v121
	v_cvt_pk_bf16_f32 v117, v122, v123
	v_cvt_pk_bf16_f32 v118, v118, v119
	v_cvt_pk_bf16_f32 v119, v124, v125
	ds_bpermute_b32 v244, v248, v116
	ds_bpermute_b32 v245, v248, v117
	ds_bpermute_b32 v246, v248, v118
	ds_bpermute_b32 v247, v248, v119
	s_waitcnt lgkmcnt(4)
; #define PG8_ST16(rs, b0, p, v) __builtin_amdgcn_raw_buffer_store_b128(v, rs, (int)((const char*)(p) - (const char*)(b0)), 0, 16)
; __device__ __forceinline__ unsigned cvt_pk_bf16(float lo, float hi) { unsigned r; asm volatile("v_cvt_pk_bf16_f32 %0, %1, %2" : "=v"(r) : "v"(lo), "v"(hi)); return r; }
;     __device__ __forceinline__ void operator()(const f32x4 (&acc)[2][2][4][2], const Unit& u, int wr, int wc, int fr, int fq) const {
;     ...
;             for (int m = 0; m < 4; ++m) { const size_t off = (size_t)(row0 + ai * HALF + m * 16) * ldc + col0; float ssq = 0.f;
; #pragma unroll
;                 for (int bj = 0; bj < 2; ++bj) {
;                     const f32x4 o0 = b0[m][bj] + acc[ai][bj][m][0] * sc, o1 = b1[m][bj] + acc[ai][bj][m][1] * sc;
;                     ssq += ((o0[0] * o0[0] + o0[1] * o0[1]) + (o0[2] * o0[2] + o0[3] * o0[3])) + ((o1[0] * o1[0] + o1[1] * o1[1]) + (o1[2] * o1[2] + o1[3] * o1[3]));
;                     u32x4 w; w.x = cvt_pk_bf16(o0[0], o0[1]); w.y = cvt_pk_bf16(o0[2], o0[3]); w.z = cvt_pk_bf16(o1[0], o1[1]); w.w = cvt_pk_bf16(o1[2], o1[3]);
;                     PG8_ST16(rs_, out, out + off + bj * HALF, w); }
;                 ssq += __shfl_xor(ssq, 16); ssq += __shfl_xor(ssq, 32);
;                 if (fq == 0) rowss[(size_t)(row0 + ai * HALF + m * 16) * 32 + 4 * u.pn + wc] = ssq; }
	global_store_dwordx4 v[234:235], v[240:243], off
	s_nop 1
	v_and_b32_e32 v117, 64, v215
	v_xor_b32_e32 v116, 16, v215
	v_add_u32_e32 v117, 64, v117
	v_cmp_lt_i32_e32 vcc, v116, v117
	v_xor_b32_e32 v118, 32, v215
	s_nop 0
	v_cndmask_b32_e32 v116, v215, v116, vcc
	v_lshlrev_b32_e32 v220, 2, v116
	ds_bpermute_b32 v116, v220, v126
	v_cmp_lt_i32_e32 vcc, v118, v117
	s_waitcnt lgkmcnt(0)
	v_add_f32_e32 v116, v126, v116
	v_cndmask_b32_e32 v117, v215, v118, vcc
	v_lshlrev_b32_e32 v221, 2, v117
	ds_bpermute_b32 v117, v221, v116
	s_and_saveexec_b64 s[44:45], s[2:3]
	s_cbranch_execz .LBB0_873
	v_lshlrev_b64 v[118:119], 7, v[194:195]
	v_lshl_add_u64 v[118:119], s[22:23], 0, v[118:119]
	v_lshl_add_u64 v[118:119], s[42:43], 2, v[118:119]
	s_lshl_b32 s68, s60, 2
	s_mov_b32 s69, s31
	v_lshl_add_u64 v[118:119], v[118:119], 0, s[68:69]
	s_waitcnt lgkmcnt(0)
	v_add_f32_e32 v116, v116, v117
	global_store_dword v[118:119], v116, off
.LBB0_873:
	s_or_b64 exec, exec, s[44:45]
	v_pk_add_f32 v[114:115], v[114:115], v[178:179]
	v_pk_add_f32 v[112:113], v[112:113], v[176:177]
	v_pk_add_f32 v[118:119], v[110:111], v[174:175]
	v_pk_add_f32 v[110:111], v[108:109], v[172:173]
	v_mul_f32_e32 v108, v113, v113
	v_mul_f32_e32 v109, v115, v115
	v_fmac_f32_e32 v108, v112, v112
	v_fmac_f32_e32 v109, v114, v114
	v_add_f32_e32 v108, v108, v109
	v_mul_f32_e32 v109, v111, v111
	v_mul_f32_e32 v120, v119, v119
	v_fmac_f32_e32 v109, v110, v110
	v_fmac_f32_e32 v120, v118, v118
	v_add_f32_e32 v109, v109, v120
	v_pk_add_f32 v[106:107], v[106:107], v[170:171]
	v_pk_add_f32 v[104:105], v[104:105], v[168:169]
	v_add_f32_e32 v120, v108, v109
	v_cvt_pk_bf16_f32 v108, v112, v113
	v_cvt_pk_bf16_f32 v109, v114, v115
	v_pk_add_f32 v[114:115], v[100:101], v[164:165]
	v_mul_f32_e32 v100, v105, v105
	v_mul_f32_e32 v101, v107, v107
	v_pk_add_f32 v[112:113], v[102:103], v[166:167]
	v_fmac_f32_e32 v100, v104, v104
	v_fmac_f32_e32 v101, v106, v106
	v_add_f32_e32 v100, v100, v101
	v_mul_f32_e32 v101, v115, v115
	v_mul_f32_e32 v102, v113, v113
	v_fmac_f32_e32 v101, v114, v114
	v_fmac_f32_e32 v102, v112, v112
	v_add_f32_e32 v101, v101, v102
	v_add_f32_e32 v100, v100, v101
	v_add_f32_e32 v103, v120, v100
	v_cvt_pk_bf16_f32 v110, v110, v111
	v_cvt_pk_bf16_f32 v111, v118, v119
	ds_bpermute_b32 v118, v220, v103
	s_waitcnt lgkmcnt(1)
	v_lshlrev_b64 v[116:117], 11, v[204:205]
	v_lshl_add_u64 v[100:101], v[116:117], 1, s[20:21]
	v_lshl_add_u64 v[116:117], v[190:191], 1, v[100:101]
	v_lshl_add_u64 v[236:237], v[116:117], 0, v[238:239]
	ds_bpermute_b32 v240, v248, v108
	ds_bpermute_b32 v241, v248, v109
	ds_bpermute_b32 v242, v248, v110
	ds_bpermute_b32 v243, v248, v111
	s_waitcnt lgkmcnt(4)
	global_store_dwordx4 v[234:235], v[244:247], off offset:256
	s_waitcnt lgkmcnt(0)
	v_add_f32_e32 v100, v103, v118
	ds_bpermute_b32 v101, v221, v100
	v_cvt_pk_bf16_f32 v102, v104, v105
	v_cvt_pk_bf16_f32 v103, v106, v107
	v_cvt_pk_bf16_f32 v104, v114, v115
	v_cvt_pk_bf16_f32 v105, v112, v113
	ds_bpermute_b32 v244, v248, v102
	ds_bpermute_b32 v245, v248, v103
	ds_bpermute_b32 v246, v248, v104
	ds_bpermute_b32 v247, v248, v105
	s_waitcnt lgkmcnt(4)
	global_store_dwordx4 v[236:237], v[240:243], off
	s_and_saveexec_b64 s[44:45], s[2:3]
	s_cbranch_execz .LBB0_875
	v_lshlrev_b64 v[102:103], 7, v[204:205]
	v_lshl_add_u64 v[102:103], s[22:23], 0, v[102:103]
	v_lshl_add_u64 v[102:103], s[42:43], 2, v[102:103]
	s_lshl_b32 s68, s60, 2
	s_mov_b32 s69, s31
	v_lshl_add_u64 v[102:103], v[102:103], 0, s[68:69]
	s_waitcnt lgkmcnt(0)
	v_add_f32_e32 v100, v100, v101
	global_store_dword v[102:103], v100, off
.LBB0_875:
	s_or_b64 exec, exec, s[44:45]
	v_pk_add_f32 v[98:99], v[98:99], v[162:163]
	v_pk_add_f32 v[96:97], v[96:97], v[160:161]
	v_pk_add_f32 v[102:103], v[94:95], v[158:159]
	v_pk_add_f32 v[94:95], v[92:93], v[156:157]
	v_mul_f32_e32 v92, v97, v97
	v_mul_f32_e32 v93, v99, v99
	v_fmac_f32_e32 v92, v96, v96
	v_fmac_f32_e32 v93, v98, v98
	v_add_f32_e32 v92, v92, v93
	v_mul_f32_e32 v93, v95, v95
	v_mul_f32_e32 v104, v103, v103
	v_fmac_f32_e32 v93, v94, v94
	v_fmac_f32_e32 v104, v102, v102
	v_add_f32_e32 v93, v93, v104
	v_pk_add_f32 v[90:91], v[90:91], v[150:151]
	v_pk_add_f32 v[88:89], v[88:89], v[148:149]
	v_add_f32_e32 v104, v92, v93
	v_cvt_pk_bf16_f32 v92, v96, v97
	v_cvt_pk_bf16_f32 v93, v98, v99
	v_pk_add_f32 v[98:99], v[84:85], v[140:141]
	v_mul_f32_e32 v84, v89, v89
	v_mul_f32_e32 v85, v91, v91
	v_pk_add_f32 v[96:97], v[86:87], v[142:143]
	v_fmac_f32_e32 v84, v88, v88
	v_fmac_f32_e32 v85, v90, v90
	v_add_f32_e32 v84, v84, v85
	v_mul_f32_e32 v85, v99, v99
	v_mul_f32_e32 v86, v97, v97
	v_fmac_f32_e32 v85, v98, v98
	v_fmac_f32_e32 v86, v96, v96
	v_add_f32_e32 v85, v85, v86
	v_add_f32_e32 v84, v84, v85
	v_add_f32_e32 v87, v104, v84
	v_cvt_pk_bf16_f32 v94, v94, v95
	v_cvt_pk_bf16_f32 v95, v102, v103
	ds_bpermute_b32 v102, v220, v87
	s_waitcnt lgkmcnt(1)
	v_lshlrev_b64 v[100:101], 11, v[202:203]
	v_lshl_add_u64 v[84:85], v[100:101], 1, s[20:21]
	v_lshl_add_u64 v[100:101], v[190:191], 1, v[84:85]
	v_lshl_add_u64 v[234:235], v[100:101], 0, v[238:239]
	ds_bpermute_b32 v240, v248, v92
	ds_bpermute_b32 v241, v248, v93
	ds_bpermute_b32 v242, v248, v94
	ds_bpermute_b32 v243, v248, v95
	s_waitcnt lgkmcnt(4)
	global_store_dwordx4 v[236:237], v[244:247], off offset:256
	s_waitcnt lgkmcnt(0)
	v_add_f32_e32 v84, v87, v102
	ds_bpermute_b32 v85, v221, v84
	v_cvt_pk_bf16_f32 v86, v88, v89
	v_cvt_pk_bf16_f32 v87, v90, v91
	v_cvt_pk_bf16_f32 v88, v98, v99
	v_cvt_pk_bf16_f32 v89, v96, v97
	ds_bpermute_b32 v244, v248, v86
	ds_bpermute_b32 v245, v248, v87
	ds_bpermute_b32 v246, v248, v88
	ds_bpermute_b32 v247, v248, v89
	s_waitcnt lgkmcnt(4)
	global_store_dwordx4 v[234:235], v[240:243], off
	s_and_saveexec_b64 s[44:45], s[2:3]
	s_cbranch_execz .LBB0_877
	v_lshlrev_b64 v[86:87], 7, v[202:203]
	v_lshl_add_u64 v[86:87], s[22:23], 0, v[86:87]
	v_lshl_add_u64 v[86:87], s[42:43], 2, v[86:87]
	s_lshl_b32 s68, s60, 2
	s_mov_b32 s69, s31
	v_lshl_add_u64 v[86:87], v[86:87], 0, s[68:69]
	s_waitcnt lgkmcnt(0)
	v_add_f32_e32 v84, v84, v85
	global_store_dword v[86:87], v84, off
; #define PG8_ST16(rs, b0, p, v) __builtin_amdgcn_raw_buffer_store_b128(v, rs, (int)((const char*)(p) - (const char*)(b0)), 0, 16)
; __device__ __forceinline__ unsigned cvt_pk_bf16(float lo, float hi) { unsigned r; asm volatile("v_cvt_pk_bf16_f32 %0, %1, %2" : "=v"(r) : "v"(lo), "v"(hi)); return r; }
;     __device__ __forceinline__ void operator()(const f32x4 (&acc)[2][2][4][2], const Unit& u, int wr, int wc, int fr, int fq) const {
;     ...
;             for (int m = 0; m < 4; ++m) { const size_t off = (size_t)(row0 + ai * HALF + m * 16) * ldc + col0;
; #pragma unroll
;                 for (int bj = 0; bj < 2; ++bj) {
;                     if (BASE_F32) { b0[m][bj] = *(const f32x4*)((const float*)base + off + bj * HALF); b1[m][bj] = *(const f32x4*)((const float*)base + off + bj * HALF + 4); }
;                     else { const u32x4 q = *(const u32x4*)((const bf16_t*)base + off + bj * HALF);
;                         b0[m][bj] = (f32x4){__uint_as_float(q.x << 16), __uint_as_float(q.x & 0xffff0000u), __uint_as_float(q.y << 16), __uint_as_float(q.y & 0xffff0000u)};
;                         b1[m][bj] = (f32x4){__uint_as_float(q.z << 16), __uint_as_float(q.z & 0xffff0000u), __uint_as_float(q.w << 16), __uint_as_float(q.w & 0xffff0000u)}; } } }
;             asm volatile("" ::: "memory");
; #pragma unroll
;             for (int m = 0; m < 4; ++m) { const size_t off = (size_t)(row0 + ai * HALF + m * 16) * ldc + col0; float ssq = 0.f;
; #pragma unroll
;                 for (int bj = 0; bj < 2; ++bj) {
;                     const f32x4 o0 = b0[m][bj] + acc[ai][bj][m][0] * sc, o1 = b1[m][bj] + acc[ai][bj][m][1] * sc;
;                     ssq += ((o0[0] * o0[0] + o0[1] * o0[1]) + (o0[2] * o0[2] + o0[3] * o0[3])) + ((o1[0] * o1[0] + o1[1] * o1[1]) + (o1[2] * o1[2] + o1[3] * o1[3]));
;                     u32x4 w; w.x = cvt_pk_bf16(o0[0], o0[1]); w.y = cvt_pk_bf16(o0[2], o0[3]); w.z = cvt_pk_bf16(o1[0], o1[1]); w.w = cvt_pk_bf16(o1[2], o1[3]);
;                     PG8_ST16(rs_, out, out + off + bj * HALF, w); }
;                 ssq += __shfl_xor(ssq, 16); ssq += __shfl_xor(ssq, 32);
;                 if (fq == 0) rowss[(size_t)(row0 + ai * HALF + m * 16) * 32 + 4 * u.pn + wc] = ssq; }
.LBB0_877:
	s_or_b64 exec, exec, s[44:45]
	v_pk_add_f32 v[82:83], v[82:83], v[154:155]
	v_pk_add_f32 v[80:81], v[80:81], v[152:153]
	v_pk_add_f32 v[86:87], v[78:79], v[146:147]
	v_pk_add_f32 v[78:79], v[76:77], v[144:145]
	v_mul_f32_e32 v76, v81, v81
	v_mul_f32_e32 v77, v83, v83
	v_fmac_f32_e32 v76, v80, v80
	v_fmac_f32_e32 v77, v82, v82
	v_add_f32_e32 v76, v76, v77
	v_mul_f32_e32 v77, v79, v79
	v_mul_f32_e32 v88, v87, v87
	v_fmac_f32_e32 v77, v78, v78
	v_fmac_f32_e32 v88, v86, v86
	v_add_f32_e32 v77, v77, v88
	v_pk_add_f32 v[74:75], v[74:75], v[138:139]
	v_pk_add_f32 v[72:73], v[72:73], v[136:137]
	v_add_f32_e32 v88, v76, v77
	v_cvt_pk_bf16_f32 v76, v80, v81
	v_cvt_pk_bf16_f32 v77, v82, v83
	v_pk_add_f32 v[82:83], v[68:69], v[132:133]
	v_mul_f32_e32 v68, v73, v73
	v_mul_f32_e32 v69, v75, v75
	v_pk_add_f32 v[80:81], v[70:71], v[134:135]
	v_fmac_f32_e32 v68, v72, v72
	v_fmac_f32_e32 v69, v74, v74
	v_add_f32_e32 v68, v68, v69
	v_mul_f32_e32 v69, v83, v83
	v_mul_f32_e32 v70, v81, v81
	v_fmac_f32_e32 v69, v82, v82
	v_fmac_f32_e32 v70, v80, v80
	v_add_f32_e32 v69, v69, v70
	v_add_f32_e32 v68, v68, v69
	v_add_f32_e32 v71, v88, v68
	v_cvt_pk_bf16_f32 v78, v78, v79
	v_cvt_pk_bf16_f32 v79, v86, v87
	ds_bpermute_b32 v86, v220, v71
	s_waitcnt lgkmcnt(1)
	v_lshlrev_b64 v[84:85], 11, v[196:197]
	v_lshl_add_u64 v[68:69], v[84:85], 1, s[20:21]
	v_lshl_add_u64 v[84:85], v[190:191], 1, v[68:69]
	v_lshl_add_u64 v[236:237], v[84:85], 0, v[238:239]
	ds_bpermute_b32 v240, v248, v76
	ds_bpermute_b32 v241, v248, v77
	ds_bpermute_b32 v242, v248, v78
	ds_bpermute_b32 v243, v248, v79
	s_waitcnt lgkmcnt(4)
	global_store_dwordx4 v[234:235], v[244:247], off offset:256
	s_waitcnt lgkmcnt(0)
	v_add_f32_e32 v68, v71, v86
	ds_bpermute_b32 v69, v221, v68
	v_cvt_pk_bf16_f32 v70, v72, v73
	v_cvt_pk_bf16_f32 v71, v74, v75
	v_cvt_pk_bf16_f32 v72, v82, v83
	v_cvt_pk_bf16_f32 v73, v80, v81
	ds_bpermute_b32 v244, v248, v70
	ds_bpermute_b32 v245, v248, v71
	ds_bpermute_b32 v246, v248, v72
	ds_bpermute_b32 v247, v248, v73
	s_waitcnt lgkmcnt(4)
	global_store_dwordx4 v[236:237], v[240:243], off
	s_waitcnt lgkmcnt(0)
	global_store_dwordx4 v[236:237], v[244:247], off offset:256
	s_and_saveexec_b64 s[44:45], s[2:3]
	s_cbranch_execz .LBB0_879
	v_lshlrev_b64 v[70:71], 7, v[196:197]
	v_lshl_add_u64 v[70:71], s[22:23], 0, v[70:71]
	v_lshl_add_u64 v[70:71], s[42:43], 2, v[70:71]
	s_lshl_b32 s68, s60, 2
	s_mov_b32 s69, s31
	v_lshl_add_u64 v[70:71], v[70:71], 0, s[68:69]
	s_waitcnt lgkmcnt(0)
	v_add_f32_e32 v68, v68, v69
	global_store_dword v[70:71], v68, off
.LBB0_879:
	s_or_b64 exec, exec, s[44:45]
	v_add_u32_e32 v130, 0x80, v194
	v_ashrrev_i32_e32 v131, 31, v130
	s_waitcnt lgkmcnt(0)
	v_lshlrev_b64 v[68:69], 13, v[130:131]
	v_lshl_add_u64 v[68:69], v[192:193], 0, v[68:69]
	global_load_dwordx4 v[132:135], v[68:69], off offset:16
	global_load_dwordx4 v[136:139], v[68:69], off
	global_load_dwordx4 v[116:119], v[68:69], off offset:528
	global_load_dwordx4 v[120:123], v[68:69], off offset:512
	v_add_u32_e32 v128, 0x90, v194
	v_ashrrev_i32_e32 v129, 31, v128
	v_lshlrev_b64 v[68:69], 13, v[128:129]
	v_add_u32_e32 v126, 0xa0, v194
	v_lshl_add_u64 v[68:69], v[192:193], 0, v[68:69]
	v_ashrrev_i32_e32 v127, 31, v126
	global_load_dwordx4 v[108:111], v[68:69], off offset:16
	global_load_dwordx4 v[112:115], v[68:69], off
	global_load_dwordx4 v[100:103], v[68:69], off offset:528
	global_load_dwordx4 v[104:107], v[68:69], off offset:512
	v_lshlrev_b64 v[68:69], 13, v[126:127]
	v_add_u32_e32 v124, 0xb0, v194
	v_lshl_add_u64 v[68:69], v[192:193], 0, v[68:69]
	v_ashrrev_i32_e32 v125, 31, v124
	global_load_dwordx4 v[92:95], v[68:69], off offset:16
	global_load_dwordx4 v[96:99], v[68:69], off
	global_load_dwordx4 v[76:79], v[68:69], off offset:528
	global_load_dwordx4 v[84:87], v[68:69], off offset:512
	v_lshlrev_b64 v[68:69], 13, v[124:125]
	v_lshl_add_u64 v[72:73], v[192:193], 0, v[68:69]
	global_load_dwordx4 v[80:83], v[72:73], off offset:16
	global_load_dwordx4 v[88:91], v[72:73], off
	global_load_dwordx4 v[68:71], v[72:73], off offset:528
	s_nop 0
	global_load_dwordx4 v[72:75], v[72:73], off offset:512
	s_waitcnt vmcnt(0)
	ds_bpermute_b32 v132, v249, v132
	ds_bpermute_b32 v133, v249, v133
	ds_bpermute_b32 v134, v249, v134
	ds_bpermute_b32 v135, v249, v135
	ds_bpermute_b32 v136, v249, v136
	ds_bpermute_b32 v137, v249, v137
	ds_bpermute_b32 v138, v249, v138
	ds_bpermute_b32 v139, v249, v139
	ds_bpermute_b32 v116, v249, v116
	ds_bpermute_b32 v117, v249, v117
	ds_bpermute_b32 v118, v249, v118
	ds_bpermute_b32 v119, v249, v119
	ds_bpermute_b32 v120, v249, v120
	ds_bpermute_b32 v121, v249, v121
	ds_bpermute_b32 v122, v249, v122
	ds_bpermute_b32 v123, v249, v123
	ds_bpermute_b32 v108, v249, v108
	ds_bpermute_b32 v109, v249, v109
	ds_bpermute_b32 v110, v249, v110
	ds_bpermute_b32 v111, v249, v111
	ds_bpermute_b32 v112, v249, v112
	ds_bpermute_b32 v113, v249, v113
	ds_bpermute_b32 v114, v249, v114
	ds_bpermute_b32 v115, v249, v115
	ds_bpermute_b32 v100, v249, v100
	ds_bpermute_b32 v101, v249, v101
	ds_bpermute_b32 v102, v249, v102
	ds_bpermute_b32 v103, v249, v103
	ds_bpermute_b32 v104, v249, v104
	ds_bpermute_b32 v105, v249, v105
	ds_bpermute_b32 v106, v249, v106
	ds_bpermute_b32 v107, v249, v107
	ds_bpermute_b32 v92, v249, v92
	ds_bpermute_b32 v93, v249, v93
	ds_bpermute_b32 v94, v249, v94
	ds_bpermute_b32 v95, v249, v95
	ds_bpermute_b32 v96, v249, v96
	ds_bpermute_b32 v97, v249, v97
	ds_bpermute_b32 v98, v249, v98
	ds_bpermute_b32 v99, v249, v99
	ds_bpermute_b32 v76, v249, v76
	ds_bpermute_b32 v77, v249, v77
	ds_bpermute_b32 v78, v249, v78
	ds_bpermute_b32 v79, v249, v79
	ds_bpermute_b32 v84, v249, v84
	ds_bpermute_b32 v85, v249, v85
	ds_bpermute_b32 v86, v249, v86
	ds_bpermute_b32 v87, v249, v87
	ds_bpermute_b32 v80, v249, v80
	ds_bpermute_b32 v81, v249, v81
	ds_bpermute_b32 v82, v249, v82
	ds_bpermute_b32 v83, v249, v83
	ds_bpermute_b32 v88, v249, v88
	ds_bpermute_b32 v89, v249, v89
	ds_bpermute_b32 v90, v249, v90
	ds_bpermute_b32 v91, v249, v91
	ds_bpermute_b32 v68, v249, v68
	ds_bpermute_b32 v69, v249, v69
	ds_bpermute_b32 v70, v249, v70
	ds_bpermute_b32 v71, v249, v71
	ds_bpermute_b32 v72, v249, v72
	ds_bpermute_b32 v73, v249, v73
	ds_bpermute_b32 v74, v249, v74
	ds_bpermute_b32 v75, v249, v75
	s_waitcnt lgkmcnt(0)
; #define PG8_ST16(rs, b0, p, v) __builtin_amdgcn_raw_buffer_store_b128(v, rs, (int)((const char*)(p) - (const char*)(b0)), 0, 16)
; __device__ __forceinline__ unsigned cvt_pk_bf16(float lo, float hi) { unsigned r; asm volatile("v_cvt_pk_bf16_f32 %0, %1, %2" : "=v"(r) : "v"(lo), "v"(hi)); return r; }
;     __device__ __forceinline__ void operator()(const f32x4 (&acc)[2][2][4][2], const Unit& u, int wr, int wc, int fr, int fq) const {
;     ...
;             for (int m = 0; m < 4; ++m) { const size_t off = (size_t)(row0 + ai * HALF + m * 16) * ldc + col0; float ssq = 0.f;
; #pragma unroll
;                 for (int bj = 0; bj < 2; ++bj) {
;                     const f32x4 o0 = b0[m][bj] + acc[ai][bj][m][0] * sc, o1 = b1[m][bj] + acc[ai][bj][m][1] * sc;
;                     ssq += ((o0[0] * o0[0] + o0[1] * o0[1]) + (o0[2] * o0[2] + o0[3] * o0[3])) + ((o1[0] * o1[0] + o1[1] * o1[1]) + (o1[2] * o1[2] + o1[3] * o1[3]));
;                     u32x4 w; w.x = cvt_pk_bf16(o0[0], o0[1]); w.y = cvt_pk_bf16(o0[2], o0[3]); w.z = cvt_pk_bf16(o1[0], o1[1]); w.w = cvt_pk_bf16(o1[2], o1[3]);
;                     PG8_ST16(rs_, out, out + off + bj * HALF, w); }
;                 ssq += __shfl_xor(ssq, 16); ssq += __shfl_xor(ssq, 32);
;                 if (fq == 0) rowss[(size_t)(row0 + ai * HALF + m * 16) * 32 + 4 * u.pn + wc] = ssq; }
	v_pk_add_f32 v[134:135], v[62:63], v[134:135]
	s_waitcnt vmcnt(14)
	v_pk_add_f32 v[66:67], v[66:67], v[138:139]
	v_pk_add_f32 v[64:65], v[64:65], v[136:137]
	v_pk_add_f32 v[62:63], v[60:61], v[132:133]
	v_mul_f32_e32 v60, v65, v65
	v_mul_f32_e32 v61, v67, v67
	v_fmac_f32_e32 v60, v64, v64
	v_fmac_f32_e32 v61, v66, v66
	v_add_f32_e32 v60, v60, v61
	v_mul_f32_e32 v61, v63, v63
	v_mul_f32_e32 v132, v135, v135
	v_fmac_f32_e32 v61, v62, v62
	v_fmac_f32_e32 v132, v134, v134
	v_add_f32_e32 v61, v61, v132
	v_add_f32_e32 v132, v60, v61
	v_cvt_pk_bf16_f32 v60, v64, v65
	v_lshlrev_b64 v[64:65], 12, v[130:131]
	v_lshl_add_u64 v[64:65], s[20:21], 0, v[64:65]
	v_cvt_pk_bf16_f32 v61, v66, v67
	v_lshl_add_u64 v[64:65], v[190:191], 1, v[64:65]
	s_waitcnt vmcnt(12)
	v_pk_add_f32 v[58:59], v[58:59], v[122:123]
	v_pk_add_f32 v[56:57], v[56:57], v[120:121]
	v_cvt_pk_bf16_f32 v62, v62, v63
	v_cvt_pk_bf16_f32 v63, v134, v135
	v_lshl_add_u64 v[234:235], v[64:65], 0, v[238:239]
	ds_bpermute_b32 v240, v248, v60
	ds_bpermute_b32 v241, v248, v61
	ds_bpermute_b32 v242, v248, v62
	ds_bpermute_b32 v243, v248, v63
	s_nop 1
	v_pk_add_f32 v[60:61], v[54:55], v[118:119]
	v_pk_add_f32 v[54:55], v[52:53], v[116:117]
	v_mul_f32_e32 v52, v57, v57
	v_mul_f32_e32 v53, v59, v59
	v_fmac_f32_e32 v52, v56, v56
	v_fmac_f32_e32 v53, v58, v58
	v_add_f32_e32 v52, v52, v53
	v_mul_f32_e32 v53, v55, v55
	v_mul_f32_e32 v62, v61, v61
	v_fmac_f32_e32 v53, v54, v54
	v_fmac_f32_e32 v62, v60, v60
	v_add_f32_e32 v53, v53, v62
	v_add_f32_e32 v52, v52, v53
	v_add_f32_e32 v62, v132, v52
	v_cvt_pk_bf16_f32 v52, v56, v57
	v_cvt_pk_bf16_f32 v53, v58, v59
	v_cvt_pk_bf16_f32 v54, v54, v55
	v_cvt_pk_bf16_f32 v55, v60, v61
	ds_bpermute_b32 v244, v248, v52
	ds_bpermute_b32 v245, v248, v53
	ds_bpermute_b32 v246, v248, v54
	ds_bpermute_b32 v247, v248, v55
	s_waitcnt lgkmcnt(4)
	global_store_dwordx4 v[234:235], v[240:243], off
	ds_bpermute_b32 v52, v220, v62
	s_waitcnt lgkmcnt(0)
	v_add_f32_e32 v52, v62, v52
	ds_bpermute_b32 v53, v221, v52
	s_and_saveexec_b64 s[44:45], s[2:3]
	s_cbranch_execz .LBB0_881
	v_lshlrev_b64 v[54:55], 7, v[130:131]
	v_lshl_add_u64 v[54:55], s[22:23], 0, v[54:55]
	v_lshl_add_u64 v[54:55], s[42:43], 2, v[54:55]
	s_lshl_b32 s68, s60, 2
	s_mov_b32 s69, s31
	v_lshl_add_u64 v[54:55], v[54:55], 0, s[68:69]
	s_waitcnt lgkmcnt(0)
	v_add_f32_e32 v52, v52, v53
	global_store_dword v[54:55], v52, off
.LBB0_881:
	s_or_b64 exec, exec, s[44:45]
	s_waitcnt vmcnt(12)
	v_pk_add_f32 v[50:51], v[50:51], v[114:115]
	v_pk_add_f32 v[48:49], v[48:49], v[112:113]
	v_pk_add_f32 v[54:55], v[46:47], v[110:111]
	v_pk_add_f32 v[46:47], v[44:45], v[108:109]
	v_mul_f32_e32 v44, v49, v49
	v_mul_f32_e32 v45, v51, v51
	v_fmac_f32_e32 v44, v48, v48
	v_fmac_f32_e32 v45, v50, v50
	v_add_f32_e32 v44, v44, v45
	v_mul_f32_e32 v45, v47, v47
	v_mul_f32_e32 v56, v55, v55
	v_fmac_f32_e32 v45, v46, v46
	v_fmac_f32_e32 v56, v54, v54
	v_add_f32_e32 v45, v45, v56
	s_waitcnt vmcnt(10)
	v_pk_add_f32 v[42:43], v[42:43], v[106:107]
	v_pk_add_f32 v[40:41], v[40:41], v[104:105]
	v_add_f32_e32 v56, v44, v45
	v_cvt_pk_bf16_f32 v44, v48, v49
	v_cvt_pk_bf16_f32 v45, v50, v51
	v_pk_add_f32 v[50:51], v[36:37], v[100:101]
	v_mul_f32_e32 v36, v41, v41
	v_mul_f32_e32 v37, v43, v43
	v_pk_add_f32 v[48:49], v[38:39], v[102:103]
	v_fmac_f32_e32 v36, v40, v40
	v_fmac_f32_e32 v37, v42, v42
	v_add_f32_e32 v36, v36, v37
	v_mul_f32_e32 v37, v51, v51
	v_mul_f32_e32 v38, v49, v49
	v_fmac_f32_e32 v37, v50, v50
	v_fmac_f32_e32 v38, v48, v48
	v_add_f32_e32 v37, v37, v38
	v_add_f32_e32 v36, v36, v37
	v_add_f32_e32 v39, v56, v36
	v_cvt_pk_bf16_f32 v46, v46, v47
	v_cvt_pk_bf16_f32 v47, v54, v55
	ds_bpermute_b32 v54, v220, v39
	s_waitcnt lgkmcnt(1)
	v_lshlrev_b64 v[52:53], 11, v[128:129]
	v_lshl_add_u64 v[36:37], v[52:53], 1, s[20:21]
	v_lshl_add_u64 v[52:53], v[190:191], 1, v[36:37]
	v_lshl_add_u64 v[236:237], v[52:53], 0, v[238:239]
	ds_bpermute_b32 v240, v248, v44
	ds_bpermute_b32 v241, v248, v45
	ds_bpermute_b32 v242, v248, v46
	ds_bpermute_b32 v243, v248, v47
	s_waitcnt lgkmcnt(4)
	global_store_dwordx4 v[234:235], v[244:247], off offset:256
	s_waitcnt lgkmcnt(0)
	v_add_f32_e32 v36, v39, v54
	ds_bpermute_b32 v37, v221, v36
	v_cvt_pk_bf16_f32 v38, v40, v41
	v_cvt_pk_bf16_f32 v39, v42, v43
	v_cvt_pk_bf16_f32 v40, v50, v51
	v_cvt_pk_bf16_f32 v41, v48, v49
	ds_bpermute_b32 v244, v248, v38
	ds_bpermute_b32 v245, v248, v39
	ds_bpermute_b32 v246, v248, v40
	ds_bpermute_b32 v247, v248, v41
	s_waitcnt lgkmcnt(4)
	global_store_dwordx4 v[236:237], v[240:243], off
	s_and_saveexec_b64 s[44:45], s[2:3]
	s_cbranch_execz .LBB0_883
	v_lshlrev_b64 v[38:39], 7, v[128:129]
	v_lshl_add_u64 v[38:39], s[22:23], 0, v[38:39]
	v_lshl_add_u64 v[38:39], s[42:43], 2, v[38:39]
	s_lshl_b32 s68, s60, 2
	s_mov_b32 s69, s31
	v_lshl_add_u64 v[38:39], v[38:39], 0, s[68:69]
	s_waitcnt lgkmcnt(0)
	v_add_f32_e32 v36, v36, v37
	global_store_dword v[38:39], v36, off
; #define PG8_ST16(rs, b0, p, v) __builtin_amdgcn_raw_buffer_store_b128(v, rs, (int)((const char*)(p) - (const char*)(b0)), 0, 16)
; __device__ __forceinline__ unsigned cvt_pk_bf16(float lo, float hi) { unsigned r; asm volatile("v_cvt_pk_bf16_f32 %0, %1, %2" : "=v"(r) : "v"(lo), "v"(hi)); return r; }
;     __device__ __forceinline__ void operator()(const f32x4 (&acc)[2][2][4][2], const Unit& u, int wr, int wc, int fr, int fq) const {
;     ...
;             for (int m = 0; m < 4; ++m) { const size_t off = (size_t)(row0 + ai * HALF + m * 16) * ldc + col0; float ssq = 0.f;
; #pragma unroll
;                 for (int bj = 0; bj < 2; ++bj) {
;                     const f32x4 o0 = b0[m][bj] + acc[ai][bj][m][0] * sc, o1 = b1[m][bj] + acc[ai][bj][m][1] * sc;
;                     ssq += ((o0[0] * o0[0] + o0[1] * o0[1]) + (o0[2] * o0[2] + o0[3] * o0[3])) + ((o1[0] * o1[0] + o1[1] * o1[1]) + (o1[2] * o1[2] + o1[3] * o1[3]));
;                     u32x4 w; w.x = cvt_pk_bf16(o0[0], o0[1]); w.y = cvt_pk_bf16(o0[2], o0[3]); w.z = cvt_pk_bf16(o1[0], o1[1]); w.w = cvt_pk_bf16(o1[2], o1[3]);
;                     PG8_ST16(rs_, out, out + off + bj * HALF, w); }
;                 ssq += __shfl_xor(ssq, 16); ssq += __shfl_xor(ssq, 32);
;                 if (fq == 0) rowss[(size_t)(row0 + ai * HALF + m * 16) * 32 + 4 * u.pn + wc] = ssq; }
.LBB0_883:
	s_or_b64 exec, exec, s[44:45]
	s_waitcnt vmcnt(10)
	v_pk_add_f32 v[34:35], v[34:35], v[98:99]
	v_pk_add_f32 v[32:33], v[32:33], v[96:97]
	v_pk_add_f32 v[38:39], v[30:31], v[94:95]
	v_pk_add_f32 v[30:31], v[28:29], v[92:93]
	v_mul_f32_e32 v28, v33, v33
	v_mul_f32_e32 v29, v35, v35
	v_fmac_f32_e32 v28, v32, v32
	v_fmac_f32_e32 v29, v34, v34
	v_add_f32_e32 v28, v28, v29
	v_mul_f32_e32 v29, v31, v31
	v_mul_f32_e32 v40, v39, v39
	v_fmac_f32_e32 v29, v30, v30
	v_fmac_f32_e32 v40, v38, v38
	v_add_f32_e32 v29, v29, v40
	s_waitcnt vmcnt(8)
	v_pk_add_f32 v[26:27], v[26:27], v[86:87]
	v_pk_add_f32 v[24:25], v[24:25], v[84:85]
	v_add_f32_e32 v40, v28, v29
	v_cvt_pk_bf16_f32 v28, v32, v33
	v_cvt_pk_bf16_f32 v29, v34, v35
	v_pk_add_f32 v[34:35], v[20:21], v[76:77]
	v_mul_f32_e32 v20, v25, v25
	v_mul_f32_e32 v21, v27, v27
	v_pk_add_f32 v[32:33], v[22:23], v[78:79]
	v_fmac_f32_e32 v20, v24, v24
	v_fmac_f32_e32 v21, v26, v26
	v_add_f32_e32 v20, v20, v21
	v_mul_f32_e32 v21, v35, v35
	v_mul_f32_e32 v22, v33, v33
	v_fmac_f32_e32 v21, v34, v34
	v_fmac_f32_e32 v22, v32, v32
	v_add_f32_e32 v21, v21, v22
	v_add_f32_e32 v20, v20, v21
	v_add_f32_e32 v23, v40, v20
	v_cvt_pk_bf16_f32 v30, v30, v31
	v_cvt_pk_bf16_f32 v31, v38, v39
	ds_bpermute_b32 v38, v220, v23
	s_waitcnt lgkmcnt(1)
	v_lshlrev_b64 v[36:37], 11, v[126:127]
	v_lshl_add_u64 v[20:21], v[36:37], 1, s[20:21]
	v_lshl_add_u64 v[36:37], v[190:191], 1, v[20:21]
	v_lshl_add_u64 v[234:235], v[36:37], 0, v[238:239]
	ds_bpermute_b32 v240, v248, v28
	ds_bpermute_b32 v241, v248, v29
	ds_bpermute_b32 v242, v248, v30
	ds_bpermute_b32 v243, v248, v31
	s_waitcnt lgkmcnt(4)
	global_store_dwordx4 v[236:237], v[244:247], off offset:256
	s_waitcnt lgkmcnt(0)
	v_add_f32_e32 v20, v23, v38
	ds_bpermute_b32 v21, v221, v20
	v_cvt_pk_bf16_f32 v22, v24, v25
	v_cvt_pk_bf16_f32 v23, v26, v27
	v_cvt_pk_bf16_f32 v24, v34, v35
	v_cvt_pk_bf16_f32 v25, v32, v33
	ds_bpermute_b32 v244, v248, v22
	ds_bpermute_b32 v245, v248, v23
	ds_bpermute_b32 v246, v248, v24
	ds_bpermute_b32 v247, v248, v25
	s_waitcnt lgkmcnt(4)
	global_store_dwordx4 v[234:235], v[240:243], off
	s_and_saveexec_b64 s[44:45], s[2:3]
	s_cbranch_execz .LBB0_885
	v_lshlrev_b64 v[22:23], 7, v[126:127]
	v_lshl_add_u64 v[22:23], s[22:23], 0, v[22:23]
	v_lshl_add_u64 v[22:23], s[42:43], 2, v[22:23]
	s_lshl_b32 s68, s60, 2
	s_mov_b32 s69, s31
	v_lshl_add_u64 v[22:23], v[22:23], 0, s[68:69]
	s_waitcnt lgkmcnt(0)
	v_add_f32_e32 v20, v20, v21
	global_store_dword v[22:23], v20, off
.LBB0_885:
	s_or_b64 exec, exec, s[44:45]
	s_waitcnt vmcnt(8)
	v_pk_add_f32 v[18:19], v[18:19], v[90:91]
	v_pk_add_f32 v[16:17], v[16:17], v[88:89]
	v_pk_add_f32 v[22:23], v[14:15], v[82:83]
	v_pk_add_f32 v[14:15], v[12:13], v[80:81]
	v_mul_f32_e32 v12, v17, v17
	v_mul_f32_e32 v13, v19, v19
	v_fmac_f32_e32 v12, v16, v16
	v_fmac_f32_e32 v13, v18, v18
	v_add_f32_e32 v12, v12, v13
	v_mul_f32_e32 v13, v15, v15
	v_mul_f32_e32 v24, v23, v23
	v_fmac_f32_e32 v13, v14, v14
	v_fmac_f32_e32 v24, v22, v22
	v_add_f32_e32 v13, v13, v24
	s_waitcnt vmcnt(6)
	v_pk_add_f32 v[10:11], v[10:11], v[74:75]
	v_pk_add_f32 v[8:9], v[8:9], v[72:73]
	v_add_f32_e32 v24, v12, v13
	v_cvt_pk_bf16_f32 v12, v16, v17
	v_cvt_pk_bf16_f32 v13, v18, v19
	v_pk_add_f32 v[18:19], v[4:5], v[68:69]
	v_mul_f32_e32 v4, v9, v9
	v_mul_f32_e32 v5, v11, v11
	v_pk_add_f32 v[16:17], v[6:7], v[70:71]
	v_fmac_f32_e32 v4, v8, v8
	v_fmac_f32_e32 v5, v10, v10
	v_add_f32_e32 v4, v4, v5
	v_mul_f32_e32 v5, v19, v19
	v_mul_f32_e32 v6, v17, v17
	v_fmac_f32_e32 v5, v18, v18
	v_fmac_f32_e32 v6, v16, v16
	v_add_f32_e32 v5, v5, v6
	v_add_f32_e32 v4, v4, v5
	v_add_f32_e32 v7, v24, v4
	v_cvt_pk_bf16_f32 v14, v14, v15
	v_cvt_pk_bf16_f32 v15, v22, v23
	ds_bpermute_b32 v22, v220, v7
	s_waitcnt lgkmcnt(1)
	v_lshlrev_b64 v[20:21], 11, v[124:125]
	v_lshl_add_u64 v[4:5], v[20:21], 1, s[20:21]
	v_lshl_add_u64 v[20:21], v[190:191], 1, v[4:5]
	v_lshl_add_u64 v[236:237], v[20:21], 0, v[238:239]
	ds_bpermute_b32 v240, v248, v12
	ds_bpermute_b32 v241, v248, v13
	ds_bpermute_b32 v242, v248, v14
	ds_bpermute_b32 v243, v248, v15
	s_waitcnt lgkmcnt(4)
	global_store_dwordx4 v[234:235], v[244:247], off offset:256
	s_waitcnt lgkmcnt(0)
	v_add_f32_e32 v4, v7, v22
	ds_bpermute_b32 v5, v221, v4
	v_cvt_pk_bf16_f32 v6, v8, v9
	v_cvt_pk_bf16_f32 v7, v10, v11
	v_cvt_pk_bf16_f32 v8, v18, v19
	v_cvt_pk_bf16_f32 v9, v16, v17
	ds_bpermute_b32 v244, v248, v6
	ds_bpermute_b32 v245, v248, v7
	ds_bpermute_b32 v246, v248, v8
	ds_bpermute_b32 v247, v248, v9
	s_waitcnt lgkmcnt(4)
	global_store_dwordx4 v[236:237], v[240:243], off
	s_waitcnt lgkmcnt(0)
	global_store_dwordx4 v[236:237], v[244:247], off offset:256
	s_and_saveexec_b64 s[44:45], s[2:3]
	s_cbranch_execz .LBB0_887
	v_lshlrev_b64 v[6:7], 7, v[124:125]
	v_lshl_add_u64 v[6:7], s[22:23], 0, v[6:7]
	v_lshl_add_u64 v[6:7], s[42:43], 2, v[6:7]
	s_lshl_b32 s42, s60, 2
	s_mov_b32 s43, s31
	v_lshl_add_u64 v[6:7], v[6:7], 0, s[42:43]
	s_waitcnt lgkmcnt(0)
	v_add_f32_e32 v4, v4, v5
	global_store_dword v[6:7], v4, off
